# EpiResidual (GEMM2 layers 1-3, GEMM4): second row-half residual loads issued with the first half's into unused registers; late loads become copies, their waits removed
# baseline (speedup 1.0000x reference)
; __device__ __forceinline__ unsigned cvt_pk_bf16(float lo, float hi) { unsigned r; asm volatile("v_cvt_pk_bf16_f32 %0, %1, %2" : "=v"(r) : "v"(lo), "v"(hi)); return r; }
; __device__ __forceinline__ void st_wt16(void* p, u32x4 v) { asm volatile("global_store_dwordx4 %0, %1, off sc1\n\ts_nop 1" :: "v"(p), "v"(v) : "memory"); }
;     __device__ __forceinline__ void operator()(const f32x4 (&acc)[2][2][4][2], const Unit& u, int wr, int wc, int fr, int fq) const {
;         const int row0 = u.pm * BM + wr * 64 + fr, col0 = u.pn * BM + wc * 32 + 8 * fq;
; #pragma unroll
;         for (int ai = 0; ai < 2; ++ai) {
;             u32x4 bb[4][2]; f32x4 bf0[4][2], bf1[4][2];
; #pragma unroll
;             for (int m = 0; m < 4; ++m)
; #pragma unroll
;                 for (int bj = 0; bj < 2; ++bj) { const size_t off = (size_t)(row0 + ai * HALF + m * 16) * D + col0 + bj * HALF;
;                     if constexpr (BASE_F32) { bf0[m][bj] = *(const f32x4*)(basef + off); bf1[m][bj] = *(const f32x4*)(basef + off + 4); } else bb[m][bj] = *(const u32x4*)(hb + off); }
;             u32x2 p8[4][2];
; #pragma unroll
;             for (int m = 0; m < 4; ++m) {
;                 const int row = row0 + ai * HALF + m * 16; const size_t off = (size_t)row * D + col0; float ss = 0.f;
; #pragma unroll
;                 for (int bj = 0; bj < 2; ++bj) {
;                     f32x4 h0, h1;
;                     if constexpr (BASE_F32) { h0 = bf0[m][bj]; h1 = bf1[m][bj]; }
;                     else { const u32x4 b = bb[m][bj];
;                         h0 = (f32x4){__uint_as_float(b.x << 16), __uint_as_float(b.x & 0xffff0000u), __uint_as_float(b.y << 16), __uint_as_float(b.y & 0xffff0000u)};
;                         h1 = (f32x4){__uint_as_float(b.z << 16), __uint_as_float(b.z & 0xffff0000u), __uint_as_float(b.w << 16), __uint_as_float(b.w & 0xffff0000u)}; }
;                     h0 = h0 + acc[ai][bj][m][0]; h1 = h1 + acc[ai][bj][m][1];
;                     u32x4 w; w.x = cvt_pk_bf16(h0[0], h0[1]); w.y = cvt_pk_bf16(h0[2], h0[3]); w.z = cvt_pk_bf16(h1[0], h1[1]); w.w = cvt_pk_bf16(h1[2], h1[3]);
;                     if (WT && wt) st_wt16(hb + HO + off + bj * HALF, w); else *(u32x4*)(hb + HO + off + bj * HALF) = w;
.LBB0_756:
	v_mbcnt_lo_u32_b32 v130, -1, 0
	v_mbcnt_hi_u32_b32 v130, -1, v130
	s_lshl_b32 s4, s14, 8
	v_add_u32_e32 v130, s93, v130
	s_add_i32 s4, s4, s47
	v_and_b32_e32 v194, 15, v130
	v_or_b32_e32 v168, s4, v194
	s_lshl_b32 s4, s28, 8
	v_bfe_u32 v195, v130, 4, 2
	s_or_b32 s4, s4, s48
	v_lshl_or_b32 v166, v195, 3, s4
	v_ashrrev_i32_e32 v167, 31, v166
	v_lshlrev_b64 v[188:189], 1, v[166:167]
	v_ashrrev_i32_e32 v169, 31, v168
	v_or_b32_e32 v180, 16, v168
	v_lshl_add_u64 v[170:171], s[8:9], 0, v[188:189]
	v_lshlrev_b64 v[190:191], 11, v[168:169]
	v_ashrrev_i32_e32 v181, 31, v180
	v_or_b32_e32 v176, 32, v168
	v_lshl_add_u64 v[130:131], v[170:171], 0, v[190:191]
	v_lshlrev_b64 v[182:183], 11, v[180:181]
	v_ashrrev_i32_e32 v177, 31, v176
	v_or_b32_e32 v172, 48, v168
	global_load_dwordx4 v[184:187], v[130:131], off
	global_load_dwordx4 v[154:157], v[130:131], off offset:256
	v_lshl_add_u64 v[130:131], v[170:171], 0, v[182:183]
	v_lshlrev_b64 v[178:179], 11, v[176:177]
	v_ashrrev_i32_e32 v173, 31, v172
	global_load_dwordx4 v[150:153], v[130:131], off
	global_load_dwordx4 v[146:149], v[130:131], off offset:256
	v_lshl_add_u64 v[130:131], v[170:171], 0, v[178:179]
	v_lshlrev_b64 v[174:175], 11, v[172:173]
	global_load_dwordx4 v[142:145], v[130:131], off
	global_load_dwordx4 v[138:141], v[130:131], off offset:256
	v_lshl_add_u64 v[130:131], v[170:171], 0, v[174:175]
	global_load_dwordx4 v[134:137], v[130:131], off
	s_nop 0
	global_load_dwordx4 v[130:133], v[130:131], off offset:256
	s_mov_b64 s[76:77], 0x40000
	v_lshl_add_u64 v[216:217], v[170:171], 0, v[190:191]
	v_lshl_add_u64 v[216:217], v[216:217], 0, s[76:77]
	global_load_dwordx4 v[230:233], v[216:217], off
	global_load_dwordx4 v[234:237], v[216:217], off offset:256
	v_lshl_add_u64 v[216:217], v[170:171], 0, v[182:183]
	v_lshl_add_u64 v[216:217], v[216:217], 0, s[76:77]
	global_load_dwordx4 v[238:241], v[216:217], off
	global_load_dwordx4 v[242:245], v[216:217], off offset:256
	v_lshl_add_u64 v[216:217], v[170:171], 0, v[178:179]
	v_lshl_add_u64 v[216:217], v[216:217], 0, s[76:77]
	global_load_dwordx4 v[246:249], v[216:217], off
	global_load_dwordx4 v[250:253], v[216:217], off offset:256
	v_lshl_add_u64 v[216:217], v[170:171], 0, v[174:175]
	v_lshl_add_u64 v[216:217], v[216:217], 0, s[76:77]
	global_load_dwordx4 v[222:225], v[216:217], off
	global_load_dwordx4 v[212:215], v[216:217], off offset:256
	v_lshl_add_u64 v[190:191], s[8:9], 0, v[190:191]
	v_lshl_add_u64 v[190:191], v[190:191], 0, v[188:189]
	s_and_b64 vcc, exec, s[12:13]
	s_mov_b64 s[76:77], 0x100
	s_waitcnt vmcnt(0)
	v_lshlrev_b32_e32 v188, 16, v184
	v_and_b32_e32 v189, 0xffff0000, v184
	v_lshlrev_b32_e32 v184, 16, v185
	v_and_b32_e32 v185, 0xffff0000, v185
	v_lshlrev_b32_e32 v196, 16, v186
	v_and_b32_e32 v197, 0xffff0000, v186
	v_lshlrev_b32_e32 v186, 16, v187
	v_and_b32_e32 v187, 0xffff0000, v187
	v_pk_add_f32 v[184:185], v[128:129], v[184:185]
	v_pk_add_f32 v[188:189], v[126:127], v[188:189]
	v_pk_add_f32 v[126:127], v[124:125], v[186:187]
	v_pk_add_f32 v[128:129], v[122:123], v[196:197]
	v_cvt_pk_bf16_f32 v122, v188, v189
	v_cvt_pk_bf16_f32 v123, v184, v185
	s_nop 0
	v_cvt_pk_bf16_f32 v124, v128, v129
	v_cvt_pk_bf16_f32 v125, v126, v127
	s_cbranch_vccz .LBB0_842
	global_store_dwordx4 v[190:191], v[122:125], off
	s_cbranch_execnz .LBB0_759

; __device__ __forceinline__ unsigned cvt_pk_bf16(float lo, float hi) { unsigned r; asm volatile("v_cvt_pk_bf16_f32 %0, %1, %2" : "=v"(r) : "v"(lo), "v"(hi)); return r; }
; __device__ __forceinline__ void st_wt16(void* p, u32x4 v) { asm volatile("global_store_dwordx4 %0, %1, off sc1\n\ts_nop 1" :: "v"(p), "v"(v) : "memory"); }
;     __device__ __forceinline__ void operator()(const f32x4 (&acc)[2][2][4][2], const Unit& u, int wr, int wc, int fr, int fq) const {
;     ...
;                 for (int bj = 0; bj < 2; ++bj) { const size_t off = (size_t)(row0 + ai * HALF + m * 16) * D + col0 + bj * HALF;
;                     if constexpr (BASE_F32) { bf0[m][bj] = *(const f32x4*)(basef + off); bf1[m][bj] = *(const f32x4*)(basef + off + 4); } else bb[m][bj] = *(const u32x4*)(hb + off); }
;             u32x2 p8[4][2];
; #pragma unroll
;             for (int m = 0; m < 4; ++m) {
;                 const int row = row0 + ai * HALF + m * 16; const size_t off = (size_t)row * D + col0; float ss = 0.f;
; #pragma unroll
;                 for (int bj = 0; bj < 2; ++bj) {
;                     f32x4 h0, h1;
;                     if constexpr (BASE_F32) { h0 = bf0[m][bj]; h1 = bf1[m][bj]; }
;                     else { const u32x4 b = bb[m][bj];
;                         h0 = (f32x4){__uint_as_float(b.x << 16), __uint_as_float(b.x & 0xffff0000u), __uint_as_float(b.y << 16), __uint_as_float(b.y & 0xffff0000u)};
;                         h1 = (f32x4){__uint_as_float(b.z << 16), __uint_as_float(b.z & 0xffff0000u), __uint_as_float(b.w << 16), __uint_as_float(b.w & 0xffff0000u)}; }
;                     h0 = h0 + acc[ai][bj][m][0]; h1 = h1 + acc[ai][bj][m][1];
;                     u32x4 w; w.x = cvt_pk_bf16(h0[0], h0[1]); w.y = cvt_pk_bf16(h0[2], h0[3]); w.z = cvt_pk_bf16(h1[0], h1[1]); w.w = cvt_pk_bf16(h1[2], h1[3]);
;                     if (WT && wt) st_wt16(hb + HO + off + bj * HALF, w); else *(u32x4*)(hb + HO + off + bj * HALF) = w;
.LBB0_796:
	s_or_b64 exec, exec, s[30:31]
	v_add_u32_e32 v106, 0x80, v168
	v_ashrrev_i32_e32 v107, 31, v106
	v_add_u32_e32 v102, 0x90, v168
	v_lshlrev_b64 v[112:113], 11, v[106:107]
	v_ashrrev_i32_e32 v103, 31, v102
	v_add_u32_e32 v98, 0xa0, v168
	v_lshl_add_u64 v[66:67], v[170:171], 0, v[112:113]
	v_lshlrev_b64 v[104:105], 11, v[102:103]
	v_ashrrev_i32_e32 v99, 31, v98
	v_add_u32_e32 v94, 0xb0, v168
	v_mov_b64_e32 v[108:109], v[230:231]
	v_mov_b64_e32 v[110:111], v[232:233]
	v_mov_b64_e32 v[90:91], v[234:235]
	v_mov_b64_e32 v[92:93], v[236:237]
	v_lshl_add_u64 v[66:67], v[170:171], 0, v[104:105]
	v_lshlrev_b64 v[100:101], 11, v[98:99]
	v_ashrrev_i32_e32 v95, 31, v94
	v_mov_b64_e32 v[86:87], v[238:239]
	v_mov_b64_e32 v[88:89], v[240:241]
	v_mov_b64_e32 v[82:83], v[242:243]
	v_mov_b64_e32 v[84:85], v[244:245]
	v_lshl_add_u64 v[66:67], v[170:171], 0, v[100:101]
	v_lshlrev_b64 v[96:97], 11, v[94:95]
	v_mov_b64_e32 v[78:79], v[246:247]
	v_mov_b64_e32 v[80:81], v[248:249]
	v_mov_b64_e32 v[74:75], v[250:251]
	v_mov_b64_e32 v[76:77], v[252:253]
	v_lshl_add_u64 v[66:67], v[170:171], 0, v[96:97]
	v_mov_b64_e32 v[70:71], v[222:223]
	v_mov_b64_e32 v[72:73], v[224:225]
	s_nop 0
	v_mov_b64_e32 v[66:67], v[212:213]
	v_mov_b64_e32 v[68:69], v[214:215]
	v_lshl_add_u64 v[112:113], s[8:9], 0, v[112:113]
	s_and_b64 vcc, exec, s[4:5]
	v_lshl_add_u64 v[112:113], v[166:167], 1, v[112:113]
	v_lshlrev_b32_e32 v114, 16, v108
	v_and_b32_e32 v115, 0xffff0000, v108
	v_lshlrev_b32_e32 v108, 16, v109
	v_and_b32_e32 v109, 0xffff0000, v109
	v_lshlrev_b32_e32 v116, 16, v110
	v_and_b32_e32 v117, 0xffff0000, v110
	v_lshlrev_b32_e32 v118, 16, v111
	v_and_b32_e32 v119, 0xffff0000, v111
	v_pk_add_f32 v[108:109], v[62:63], v[108:109]
	v_pk_add_f32 v[110:111], v[60:61], v[114:115]
	v_pk_add_f32 v[60:61], v[58:59], v[118:119]
	v_pk_add_f32 v[62:63], v[56:57], v[116:117]
	v_cvt_pk_bf16_f32 v56, v110, v111
	v_cvt_pk_bf16_f32 v57, v108, v109
	s_nop 0
	v_cvt_pk_bf16_f32 v58, v62, v63
	v_cvt_pk_bf16_f32 v59, v60, v61
	s_cbranch_vccnz .LBB0_850
	global_store_dwordx4 v[112:113], v[56:59], off
	s_cbranch_execnz .LBB0_799

; __device__ __forceinline__ unsigned cvt_pk_bf16(float lo, float hi) { unsigned r; asm volatile("v_cvt_pk_bf16_f32 %0, %1, %2" : "=v"(r) : "v"(lo), "v"(hi)); return r; }
; __device__ __forceinline__ void st_wt16(void* p, u32x4 v) { asm volatile("global_store_dwordx4 %0, %1, off sc1\n\ts_nop 1" :: "v"(p), "v"(v) : "memory"); }
;     __device__ __forceinline__ void operator()(const f32x4 (&acc)[2][2][4][2], const Unit& u, int wr, int wc, int fr, int fq) const {
;     ...
;                     else { const u32x4 b = bb[m][bj];
;                         h0 = (f32x4){__uint_as_float(b.x << 16), __uint_as_float(b.x & 0xffff0000u), __uint_as_float(b.y << 16), __uint_as_float(b.y & 0xffff0000u)};
;                         h1 = (f32x4){__uint_as_float(b.z << 16), __uint_as_float(b.z & 0xffff0000u), __uint_as_float(b.w << 16), __uint_as_float(b.w & 0xffff0000u)}; }
;                     h0 = h0 + acc[ai][bj][m][0]; h1 = h1 + acc[ai][bj][m][1];
;                     u32x4 w; w.x = cvt_pk_bf16(h0[0], h0[1]); w.y = cvt_pk_bf16(h0[2], h0[3]); w.z = cvt_pk_bf16(h1[0], h1[1]); w.w = cvt_pk_bf16(h1[2], h1[3]);
;                     if (WT && wt) st_wt16(hb + HO + off + bj * HALF, w); else *(u32x4*)(hb + HO + off + bj * HALF) = w;
.LBB0_799:
	v_lshlrev_b32_e32 v56, 16, v90
	v_and_b32_e32 v57, 0xffff0000, v90
	v_lshlrev_b32_e32 v58, 16, v91
	v_and_b32_e32 v59, 0xffff0000, v91
	v_lshlrev_b32_e32 v90, 16, v92
	v_and_b32_e32 v91, 0xffff0000, v92
	v_lshlrev_b32_e32 v92, 16, v93
	v_and_b32_e32 v93, 0xffff0000, v93
	v_pk_add_f32 v[54:55], v[54:55], v[58:59]
	v_pk_add_f32 v[56:57], v[52:53], v[56:57]
	v_pk_add_f32 v[52:53], v[50:51], v[92:93]
	v_pk_add_f32 v[58:59], v[48:49], v[90:91]
	s_and_b64 vcc, exec, s[4:5]
	v_lshl_add_u64 v[90:91], v[112:113], 0, s[76:77]
	v_cvt_pk_bf16_f32 v48, v56, v57
	v_cvt_pk_bf16_f32 v49, v54, v55
	v_cvt_pk_bf16_f32 v50, v58, v59
	v_cvt_pk_bf16_f32 v51, v52, v53
	s_cbranch_vccnz .LBB0_851
	global_store_dwordx4 v[90:91], v[48:51], off
	s_cbranch_execnz .LBB0_802

; __device__ __forceinline__ unsigned cvt_pk_bf16(float lo, float hi) { unsigned r; asm volatile("v_cvt_pk_bf16_f32 %0, %1, %2" : "=v"(r) : "v"(lo), "v"(hi)); return r; }
; __device__ __forceinline__ void st_wt16(void* p, u32x4 v) { asm volatile("global_store_dwordx4 %0, %1, off sc1\n\ts_nop 1" :: "v"(p), "v"(v) : "memory"); }
;     __device__ __forceinline__ void operator()(const f32x4 (&acc)[2][2][4][2], const Unit& u, int wr, int wc, int fr, int fq) const {
;     ...
;                     else { const u32x4 b = bb[m][bj];
;                         h0 = (f32x4){__uint_as_float(b.x << 16), __uint_as_float(b.x & 0xffff0000u), __uint_as_float(b.y << 16), __uint_as_float(b.y & 0xffff0000u)};
;                         h1 = (f32x4){__uint_as_float(b.z << 16), __uint_as_float(b.z & 0xffff0000u), __uint_as_float(b.w << 16), __uint_as_float(b.w & 0xffff0000u)}; }
;                     h0 = h0 + acc[ai][bj][m][0]; h1 = h1 + acc[ai][bj][m][1];
;                     u32x4 w; w.x = cvt_pk_bf16(h0[0], h0[1]); w.y = cvt_pk_bf16(h0[2], h0[3]); w.z = cvt_pk_bf16(h1[0], h1[1]); w.w = cvt_pk_bf16(h1[2], h1[3]);
;                     if (WT && wt) st_wt16(hb + HO + off + bj * HALF, w); else *(u32x4*)(hb + HO + off + bj * HALF) = w;
.LBB0_806:
	s_or_b64 exec, exec, s[30:31]
	v_lshlrev_b32_e32 v50, 16, v87
	v_and_b32_e32 v51, 0xffff0000, v87
	v_lshlrev_b32_e32 v52, 16, v88
	v_and_b32_e32 v53, 0xffff0000, v88
	v_lshlrev_b32_e32 v48, 16, v86
	v_and_b32_e32 v49, 0xffff0000, v86
	v_lshlrev_b32_e32 v54, 16, v89
	v_and_b32_e32 v55, 0xffff0000, v89
	v_pk_add_f32 v[38:39], v[38:39], v[50:51]
	v_pk_add_f32 v[50:51], v[32:33], v[52:53]
	v_lshl_add_u64 v[52:53], s[8:9], 0, v[104:105]
	v_pk_add_f32 v[48:49], v[36:37], v[48:49]
	v_pk_add_f32 v[36:37], v[34:35], v[54:55]
	s_and_b64 vcc, exec, s[4:5]
	v_lshl_add_u64 v[52:53], v[166:167], 1, v[52:53]
	v_cvt_pk_bf16_f32 v32, v48, v49
	v_cvt_pk_bf16_f32 v33, v38, v39
	v_cvt_pk_bf16_f32 v34, v50, v51
	v_cvt_pk_bf16_f32 v35, v36, v37
	s_cbranch_vccnz .LBB0_852
	global_store_dwordx4 v[52:53], v[32:35], off
	s_cbranch_execnz .LBB0_809

; __device__ __forceinline__ unsigned cvt_pk_bf16(float lo, float hi) { unsigned r; asm volatile("v_cvt_pk_bf16_f32 %0, %1, %2" : "=v"(r) : "v"(lo), "v"(hi)); return r; }
; __device__ __forceinline__ void st_wt16(void* p, u32x4 v) { asm volatile("global_store_dwordx4 %0, %1, off sc1\n\ts_nop 1" :: "v"(p), "v"(v) : "memory"); }
;     __device__ __forceinline__ void operator()(const f32x4 (&acc)[2][2][4][2], const Unit& u, int wr, int wc, int fr, int fq) const {
;     ...
;                     else { const u32x4 b = bb[m][bj];
;                         h0 = (f32x4){__uint_as_float(b.x << 16), __uint_as_float(b.x & 0xffff0000u), __uint_as_float(b.y << 16), __uint_as_float(b.y & 0xffff0000u)};
;                         h1 = (f32x4){__uint_as_float(b.z << 16), __uint_as_float(b.z & 0xffff0000u), __uint_as_float(b.w << 16), __uint_as_float(b.w & 0xffff0000u)}; }
;                     h0 = h0 + acc[ai][bj][m][0]; h1 = h1 + acc[ai][bj][m][1];
;                     u32x4 w; w.x = cvt_pk_bf16(h0[0], h0[1]); w.y = cvt_pk_bf16(h0[2], h0[3]); w.z = cvt_pk_bf16(h1[0], h1[1]); w.w = cvt_pk_bf16(h1[2], h1[3]);
;                     if (WT && wt) st_wt16(hb + HO + off + bj * HALF, w); else *(u32x4*)(hb + HO + off + bj * HALF) = w;
.LBB0_809:
	v_lshlrev_b32_e32 v32, 16, v82
	v_and_b32_e32 v33, 0xffff0000, v82
	v_lshlrev_b32_e32 v34, 16, v83
	v_and_b32_e32 v35, 0xffff0000, v83
	v_lshlrev_b32_e32 v54, 16, v84
	v_and_b32_e32 v55, 0xffff0000, v84
	v_lshlrev_b32_e32 v56, 16, v85
	v_and_b32_e32 v57, 0xffff0000, v85
	v_pk_add_f32 v[46:47], v[46:47], v[34:35]
	v_pk_add_f32 v[44:45], v[44:45], v[32:33]
	v_pk_add_f32 v[42:43], v[42:43], v[56:57]
	v_pk_add_f32 v[40:41], v[40:41], v[54:55]
	s_and_b64 vcc, exec, s[4:5]
	v_lshl_add_u64 v[52:53], v[52:53], 0, s[76:77]
	v_cvt_pk_bf16_f32 v32, v44, v45
	v_cvt_pk_bf16_f32 v33, v46, v47
	v_cvt_pk_bf16_f32 v34, v40, v41
	v_cvt_pk_bf16_f32 v35, v42, v43
	s_cbranch_vccnz .LBB0_853
	global_store_dwordx4 v[52:53], v[32:35], off
	s_cbranch_execnz .LBB0_812

; __device__ __forceinline__ unsigned cvt_pk_bf16(float lo, float hi) { unsigned r; asm volatile("v_cvt_pk_bf16_f32 %0, %1, %2" : "=v"(r) : "v"(lo), "v"(hi)); return r; }
; __device__ __forceinline__ void st_wt16(void* p, u32x4 v) { asm volatile("global_store_dwordx4 %0, %1, off sc1\n\ts_nop 1" :: "v"(p), "v"(v) : "memory"); }
;     __device__ __forceinline__ void operator()(const f32x4 (&acc)[2][2][4][2], const Unit& u, int wr, int wc, int fr, int fq) const {
;     ...
;                     else { const u32x4 b = bb[m][bj];
;                         h0 = (f32x4){__uint_as_float(b.x << 16), __uint_as_float(b.x & 0xffff0000u), __uint_as_float(b.y << 16), __uint_as_float(b.y & 0xffff0000u)};
;                         h1 = (f32x4){__uint_as_float(b.z << 16), __uint_as_float(b.z & 0xffff0000u), __uint_as_float(b.w << 16), __uint_as_float(b.w & 0xffff0000u)}; }
;                     h0 = h0 + acc[ai][bj][m][0]; h1 = h1 + acc[ai][bj][m][1];
;                     u32x4 w; w.x = cvt_pk_bf16(h0[0], h0[1]); w.y = cvt_pk_bf16(h0[2], h0[3]); w.z = cvt_pk_bf16(h1[0], h1[1]); w.w = cvt_pk_bf16(h1[2], h1[3]);
;                     if (WT && wt) st_wt16(hb + HO + off + bj * HALF, w); else *(u32x4*)(hb + HO + off + bj * HALF) = w;
.LBB0_816:
	s_or_b64 exec, exec, s[30:31]
	v_lshlrev_b32_e32 v34, 16, v79
	v_and_b32_e32 v35, 0xffff0000, v79
	v_lshlrev_b32_e32 v36, 16, v80
	v_and_b32_e32 v37, 0xffff0000, v80
	v_lshlrev_b32_e32 v32, 16, v78
	v_and_b32_e32 v33, 0xffff0000, v78
	v_lshlrev_b32_e32 v38, 16, v81
	v_and_b32_e32 v39, 0xffff0000, v81
	v_pk_add_f32 v[22:23], v[22:23], v[34:35]
	v_pk_add_f32 v[34:35], v[16:17], v[36:37]
	v_lshl_add_u64 v[36:37], s[8:9], 0, v[100:101]
	v_pk_add_f32 v[32:33], v[20:21], v[32:33]
	v_pk_add_f32 v[20:21], v[18:19], v[38:39]
	s_and_b64 vcc, exec, s[4:5]
	v_lshl_add_u64 v[36:37], v[166:167], 1, v[36:37]
	v_cvt_pk_bf16_f32 v16, v32, v33
	v_cvt_pk_bf16_f32 v17, v22, v23
	v_cvt_pk_bf16_f32 v18, v34, v35
	v_cvt_pk_bf16_f32 v19, v20, v21
	s_cbranch_vccnz .LBB0_854
	global_store_dwordx4 v[36:37], v[16:19], off
	s_cbranch_execnz .LBB0_819

; __device__ __forceinline__ unsigned cvt_pk_bf16(float lo, float hi) { unsigned r; asm volatile("v_cvt_pk_bf16_f32 %0, %1, %2" : "=v"(r) : "v"(lo), "v"(hi)); return r; }
; __device__ __forceinline__ void st_wt16(void* p, u32x4 v) { asm volatile("global_store_dwordx4 %0, %1, off sc1\n\ts_nop 1" :: "v"(p), "v"(v) : "memory"); }
;     __device__ __forceinline__ void operator()(const f32x4 (&acc)[2][2][4][2], const Unit& u, int wr, int wc, int fr, int fq) const {
;     ...
;                     else { const u32x4 b = bb[m][bj];
;                         h0 = (f32x4){__uint_as_float(b.x << 16), __uint_as_float(b.x & 0xffff0000u), __uint_as_float(b.y << 16), __uint_as_float(b.y & 0xffff0000u)};
;                         h1 = (f32x4){__uint_as_float(b.z << 16), __uint_as_float(b.z & 0xffff0000u), __uint_as_float(b.w << 16), __uint_as_float(b.w & 0xffff0000u)}; }
;                     h0 = h0 + acc[ai][bj][m][0]; h1 = h1 + acc[ai][bj][m][1];
;                     u32x4 w; w.x = cvt_pk_bf16(h0[0], h0[1]); w.y = cvt_pk_bf16(h0[2], h0[3]); w.z = cvt_pk_bf16(h1[0], h1[1]); w.w = cvt_pk_bf16(h1[2], h1[3]);
;                     if (WT && wt) st_wt16(hb + HO + off + bj * HALF, w); else *(u32x4*)(hb + HO + off + bj * HALF) = w;
.LBB0_819:
	v_lshlrev_b32_e32 v16, 16, v74
	v_and_b32_e32 v17, 0xffff0000, v74
	v_lshlrev_b32_e32 v18, 16, v75
	v_and_b32_e32 v19, 0xffff0000, v75
	v_lshlrev_b32_e32 v38, 16, v76
	v_and_b32_e32 v39, 0xffff0000, v76
	v_lshlrev_b32_e32 v40, 16, v77
	v_and_b32_e32 v41, 0xffff0000, v77
	v_pk_add_f32 v[30:31], v[30:31], v[18:19]
	v_pk_add_f32 v[28:29], v[28:29], v[16:17]
	v_pk_add_f32 v[26:27], v[26:27], v[40:41]
	v_pk_add_f32 v[24:25], v[24:25], v[38:39]
	s_and_b64 vcc, exec, s[4:5]
	v_lshl_add_u64 v[36:37], v[36:37], 0, s[76:77]
	v_cvt_pk_bf16_f32 v16, v28, v29
	v_cvt_pk_bf16_f32 v17, v30, v31
	v_cvt_pk_bf16_f32 v18, v24, v25
	v_cvt_pk_bf16_f32 v19, v26, v27
	s_cbranch_vccnz .LBB0_855
	global_store_dwordx4 v[36:37], v[16:19], off
	s_cbranch_execnz .LBB0_822

; __device__ __forceinline__ unsigned cvt_pk_bf16(float lo, float hi) { unsigned r; asm volatile("v_cvt_pk_bf16_f32 %0, %1, %2" : "=v"(r) : "v"(lo), "v"(hi)); return r; }
; __device__ __forceinline__ void st_wt16(void* p, u32x4 v) { asm volatile("global_store_dwordx4 %0, %1, off sc1\n\ts_nop 1" :: "v"(p), "v"(v) : "memory"); }
;     __device__ __forceinline__ void operator()(const f32x4 (&acc)[2][2][4][2], const Unit& u, int wr, int wc, int fr, int fq) const {
;     ...
;                     else { const u32x4 b = bb[m][bj];
;                         h0 = (f32x4){__uint_as_float(b.x << 16), __uint_as_float(b.x & 0xffff0000u), __uint_as_float(b.y << 16), __uint_as_float(b.y & 0xffff0000u)};
;                         h1 = (f32x4){__uint_as_float(b.z << 16), __uint_as_float(b.z & 0xffff0000u), __uint_as_float(b.w << 16), __uint_as_float(b.w & 0xffff0000u)}; }
;                     h0 = h0 + acc[ai][bj][m][0]; h1 = h1 + acc[ai][bj][m][1];
;                     u32x4 w; w.x = cvt_pk_bf16(h0[0], h0[1]); w.y = cvt_pk_bf16(h0[2], h0[3]); w.z = cvt_pk_bf16(h1[0], h1[1]); w.w = cvt_pk_bf16(h1[2], h1[3]);
;                     if (WT && wt) st_wt16(hb + HO + off + bj * HALF, w); else *(u32x4*)(hb + HO + off + bj * HALF) = w;
.LBB0_826:
	s_or_b64 exec, exec, s[30:31]
	v_lshlrev_b32_e32 v18, 16, v71
	v_and_b32_e32 v19, 0xffff0000, v71
	v_lshlrev_b32_e32 v20, 16, v72
	v_and_b32_e32 v21, 0xffff0000, v72
	v_lshlrev_b32_e32 v16, 16, v70
	v_and_b32_e32 v17, 0xffff0000, v70
	v_lshlrev_b32_e32 v22, 16, v73
	v_and_b32_e32 v23, 0xffff0000, v73
	v_pk_add_f32 v[6:7], v[6:7], v[18:19]
	v_pk_add_f32 v[18:19], v[0:1], v[20:21]
	v_lshl_add_u64 v[20:21], s[8:9], 0, v[96:97]
	v_pk_add_f32 v[16:17], v[4:5], v[16:17]
	v_pk_add_f32 v[4:5], v[2:3], v[22:23]
	s_and_b64 vcc, exec, s[4:5]
	v_lshl_add_u64 v[20:21], v[166:167], 1, v[20:21]
	v_cvt_pk_bf16_f32 v0, v16, v17
	v_cvt_pk_bf16_f32 v1, v6, v7
	v_cvt_pk_bf16_f32 v2, v18, v19
	v_cvt_pk_bf16_f32 v3, v4, v5
	s_cbranch_vccnz .LBB0_856
	global_store_dwordx4 v[20:21], v[0:3], off
	s_cbranch_execnz .LBB0_829

; __device__ __forceinline__ unsigned cvt_pk_bf16(float lo, float hi) { unsigned r; asm volatile("v_cvt_pk_bf16_f32 %0, %1, %2" : "=v"(r) : "v"(lo), "v"(hi)); return r; }
; __device__ __forceinline__ void st_wt16(void* p, u32x4 v) { asm volatile("global_store_dwordx4 %0, %1, off sc1\n\ts_nop 1" :: "v"(p), "v"(v) : "memory"); }
;     __device__ __forceinline__ void operator()(const f32x4 (&acc)[2][2][4][2], const Unit& u, int wr, int wc, int fr, int fq) const {
;     ...
;                     else { const u32x4 b = bb[m][bj];
;                         h0 = (f32x4){__uint_as_float(b.x << 16), __uint_as_float(b.x & 0xffff0000u), __uint_as_float(b.y << 16), __uint_as_float(b.y & 0xffff0000u)};
;                         h1 = (f32x4){__uint_as_float(b.z << 16), __uint_as_float(b.z & 0xffff0000u), __uint_as_float(b.w << 16), __uint_as_float(b.w & 0xffff0000u)}; }
;                     h0 = h0 + acc[ai][bj][m][0]; h1 = h1 + acc[ai][bj][m][1];
;                     u32x4 w; w.x = cvt_pk_bf16(h0[0], h0[1]); w.y = cvt_pk_bf16(h0[2], h0[3]); w.z = cvt_pk_bf16(h1[0], h1[1]); w.w = cvt_pk_bf16(h1[2], h1[3]);
;                     if (WT && wt) st_wt16(hb + HO + off + bj * HALF, w); else *(u32x4*)(hb + HO + off + bj * HALF) = w;
.LBB0_829:
	v_lshlrev_b32_e32 v0, 16, v66
	v_and_b32_e32 v1, 0xffff0000, v66
	v_lshlrev_b32_e32 v2, 16, v67
	v_and_b32_e32 v3, 0xffff0000, v67
	v_lshlrev_b32_e32 v22, 16, v68
	v_and_b32_e32 v23, 0xffff0000, v68
	v_lshlrev_b32_e32 v24, 16, v69
	v_and_b32_e32 v25, 0xffff0000, v69
	v_pk_add_f32 v[14:15], v[14:15], v[2:3]
	v_pk_add_f32 v[12:13], v[12:13], v[0:1]
	v_pk_add_f32 v[10:11], v[10:11], v[24:25]
	v_pk_add_f32 v[8:9], v[8:9], v[22:23]
	s_and_b64 vcc, exec, s[4:5]
	v_lshl_add_u64 v[20:21], v[20:21], 0, s[76:77]
	v_cvt_pk_bf16_f32 v0, v12, v13
	v_cvt_pk_bf16_f32 v1, v14, v15
	v_cvt_pk_bf16_f32 v2, v8, v9
	v_cvt_pk_bf16_f32 v3, v10, v11
	s_cbranch_vccnz .LBB0_857
	global_store_dwordx4 v[20:21], v[0:3], off
	s_cbranch_execnz .LBB0_832

; __device__ __forceinline__ unsigned cvt_pk_bf16(float lo, float hi) { unsigned r; asm volatile("v_cvt_pk_bf16_f32 %0, %1, %2" : "=v"(r) : "v"(lo), "v"(hi)); return r; }
; __device__ __forceinline__ void st_wt16(void* p, u32x4 v) { asm volatile("global_store_dwordx4 %0, %1, off sc1\n\ts_nop 1" :: "v"(p), "v"(v) : "memory"); }
;     __device__ __forceinline__ void operator()(const f32x4 (&acc)[2][2][4][2], const Unit& u, int wr, int wc, int fr, int fq) const {
;         const int row0 = u.pm * BM + wr * 64 + fr, col0 = u.pn * BM + wc * 32 + 8 * fq;
; #pragma unroll
;         for (int ai = 0; ai < 2; ++ai) {
;             u32x4 bb[4][2]; f32x4 bf0[4][2], bf1[4][2];
; #pragma unroll
;             for (int m = 0; m < 4; ++m)
; #pragma unroll
;                 for (int bj = 0; bj < 2; ++bj) { const size_t off = (size_t)(row0 + ai * HALF + m * 16) * D + col0 + bj * HALF;
;                     if constexpr (BASE_F32) { bf0[m][bj] = *(const f32x4*)(basef + off); bf1[m][bj] = *(const f32x4*)(basef + off + 4); } else bb[m][bj] = *(const u32x4*)(hb + off); }
;             u32x2 p8[4][2];
; #pragma unroll
;             for (int m = 0; m < 4; ++m) {
;                 const int row = row0 + ai * HALF + m * 16; const size_t off = (size_t)row * D + col0; float ss = 0.f;
; #pragma unroll
;                 for (int bj = 0; bj < 2; ++bj) {
;                     f32x4 h0, h1;
;                     if constexpr (BASE_F32) { h0 = bf0[m][bj]; h1 = bf1[m][bj]; }
;                     else { const u32x4 b = bb[m][bj];
;                         h0 = (f32x4){__uint_as_float(b.x << 16), __uint_as_float(b.x & 0xffff0000u), __uint_as_float(b.y << 16), __uint_as_float(b.y & 0xffff0000u)};
;                         h1 = (f32x4){__uint_as_float(b.z << 16), __uint_as_float(b.z & 0xffff0000u), __uint_as_float(b.w << 16), __uint_as_float(b.w & 0xffff0000u)}; }
;                     h0 = h0 + acc[ai][bj][m][0]; h1 = h1 + acc[ai][bj][m][1];
;                     u32x4 w; w.x = cvt_pk_bf16(h0[0], h0[1]); w.y = cvt_pk_bf16(h0[2], h0[3]); w.z = cvt_pk_bf16(h1[0], h1[1]); w.w = cvt_pk_bf16(h1[2], h1[3]);
;                     if (WT && wt) st_wt16(hb + HO + off + bj * HALF, w); else *(u32x4*)(hb + HO + off + bj * HALF) = w;
.LBB0_1305:
	v_mbcnt_lo_u32_b32 v130, -1, 0
	v_mbcnt_hi_u32_b32 v130, -1, v130
	s_lshl_b32 s4, s8, 8
	v_add_u32_e32 v130, s93, v130
	s_add_i32 s4, s4, s65
	v_and_b32_e32 v190, 15, v130
	v_or_b32_e32 v164, s4, v190
	s_lshl_b32 s4, s28, 8
	v_bfe_u32 v191, v130, 4, 2
	s_or_b32 s4, s4, s68
	v_lshl_or_b32 v162, v191, 3, s4
	v_ashrrev_i32_e32 v163, 31, v162
	v_lshlrev_b64 v[184:185], 1, v[162:163]
	v_ashrrev_i32_e32 v165, 31, v164
	v_or_b32_e32 v176, 16, v164
	v_lshl_add_u64 v[166:167], s[12:13], 0, v[184:185]
	v_lshlrev_b64 v[186:187], 11, v[164:165]
	v_ashrrev_i32_e32 v177, 31, v176
	v_or_b32_e32 v172, 32, v164
	v_lshl_add_u64 v[130:131], v[166:167], 0, v[186:187]
	v_lshlrev_b64 v[178:179], 11, v[176:177]
	v_ashrrev_i32_e32 v173, 31, v172
	v_or_b32_e32 v168, 48, v164
	global_load_dwordx4 v[180:183], v[130:131], off
	global_load_dwordx4 v[154:157], v[130:131], off offset:256
	v_lshl_add_u64 v[130:131], v[166:167], 0, v[178:179]
	v_lshlrev_b64 v[174:175], 11, v[172:173]
	v_ashrrev_i32_e32 v169, 31, v168
	global_load_dwordx4 v[150:153], v[130:131], off
	global_load_dwordx4 v[146:149], v[130:131], off offset:256
	v_lshl_add_u64 v[130:131], v[166:167], 0, v[174:175]
	v_lshlrev_b64 v[170:171], 11, v[168:169]
	global_load_dwordx4 v[142:145], v[130:131], off
	global_load_dwordx4 v[138:141], v[130:131], off offset:256
	v_lshl_add_u64 v[130:131], v[166:167], 0, v[170:171]
	global_load_dwordx4 v[134:137], v[130:131], off
	s_nop 0
	global_load_dwordx4 v[130:133], v[130:131], off offset:256
	s_mov_b64 s[76:77], 0x40000
	v_lshl_add_u64 v[216:217], v[166:167], 0, v[186:187]
	v_lshl_add_u64 v[216:217], v[216:217], 0, s[76:77]
	global_load_dwordx4 v[230:233], v[216:217], off
	global_load_dwordx4 v[234:237], v[216:217], off offset:256
	v_lshl_add_u64 v[216:217], v[166:167], 0, v[178:179]
	v_lshl_add_u64 v[216:217], v[216:217], 0, s[76:77]
	global_load_dwordx4 v[238:241], v[216:217], off
	global_load_dwordx4 v[242:245], v[216:217], off offset:256
	v_lshl_add_u64 v[216:217], v[166:167], 0, v[174:175]
	v_lshl_add_u64 v[216:217], v[216:217], 0, s[76:77]
	global_load_dwordx4 v[246:249], v[216:217], off
	global_load_dwordx4 v[250:253], v[216:217], off offset:256
	v_lshl_add_u64 v[216:217], v[166:167], 0, v[170:171]
	v_lshl_add_u64 v[216:217], v[216:217], 0, s[76:77]
	global_load_dwordx4 v[222:225], v[216:217], off
	global_load_dwordx4 v[212:215], v[216:217], off offset:256
	v_lshl_add_u64 v[186:187], s[12:13], 0, v[186:187]
	v_lshl_add_u64 v[184:185], v[186:187], 0, v[184:185]
	s_and_b64 vcc, exec, s[16:17]
	s_mov_b32 s71, 0x1c000
	v_readlane_b32 s80, v255, 1
	s_mov_b64 s[76:77], 0x100
	s_waitcnt vmcnt(0)
	v_lshlrev_b32_e32 v186, 16, v180
	v_and_b32_e32 v187, 0xffff0000, v180
	v_lshlrev_b32_e32 v180, 16, v181
	v_and_b32_e32 v181, 0xffff0000, v181
	v_lshlrev_b32_e32 v192, 16, v182
	v_and_b32_e32 v193, 0xffff0000, v182
	v_lshlrev_b32_e32 v194, 16, v183
	v_and_b32_e32 v195, 0xffff0000, v183
	v_pk_add_f32 v[180:181], v[128:129], v[180:181]
	v_pk_add_f32 v[182:183], v[126:127], v[186:187]
	v_pk_add_f32 v[126:127], v[124:125], v[194:195]
	v_pk_add_f32 v[128:129], v[122:123], v[192:193]
	v_cvt_pk_bf16_f32 v122, v182, v183
	v_cvt_pk_bf16_f32 v123, v180, v181
	s_nop 0
	v_cvt_pk_bf16_f32 v124, v128, v129
	v_cvt_pk_bf16_f32 v125, v126, v127
	s_cbranch_vccz .LBB0_1391
	global_store_dwordx4 v[184:185], v[122:125], off
	s_cbranch_execnz .LBB0_1308

; __device__ __forceinline__ unsigned cvt_pk_bf16(float lo, float hi) { unsigned r; asm volatile("v_cvt_pk_bf16_f32 %0, %1, %2" : "=v"(r) : "v"(lo), "v"(hi)); return r; }
; __device__ __forceinline__ void st_wt16(void* p, u32x4 v) { asm volatile("global_store_dwordx4 %0, %1, off sc1\n\ts_nop 1" :: "v"(p), "v"(v) : "memory"); }
;     __device__ __forceinline__ void operator()(const f32x4 (&acc)[2][2][4][2], const Unit& u, int wr, int wc, int fr, int fq) const {
;     ...
;                 for (int bj = 0; bj < 2; ++bj) { const size_t off = (size_t)(row0 + ai * HALF + m * 16) * D + col0 + bj * HALF;
;                     if constexpr (BASE_F32) { bf0[m][bj] = *(const f32x4*)(basef + off); bf1[m][bj] = *(const f32x4*)(basef + off + 4); } else bb[m][bj] = *(const u32x4*)(hb + off); }
;             u32x2 p8[4][2];
; #pragma unroll
;             for (int m = 0; m < 4; ++m) {
;                 const int row = row0 + ai * HALF + m * 16; const size_t off = (size_t)row * D + col0; float ss = 0.f;
; #pragma unroll
;                 for (int bj = 0; bj < 2; ++bj) {
;                     f32x4 h0, h1;
;                     if constexpr (BASE_F32) { h0 = bf0[m][bj]; h1 = bf1[m][bj]; }
;                     else { const u32x4 b = bb[m][bj];
;                         h0 = (f32x4){__uint_as_float(b.x << 16), __uint_as_float(b.x & 0xffff0000u), __uint_as_float(b.y << 16), __uint_as_float(b.y & 0xffff0000u)};
;                         h1 = (f32x4){__uint_as_float(b.z << 16), __uint_as_float(b.z & 0xffff0000u), __uint_as_float(b.w << 16), __uint_as_float(b.w & 0xffff0000u)}; }
;                     h0 = h0 + acc[ai][bj][m][0]; h1 = h1 + acc[ai][bj][m][1];
;                     u32x4 w; w.x = cvt_pk_bf16(h0[0], h0[1]); w.y = cvt_pk_bf16(h0[2], h0[3]); w.z = cvt_pk_bf16(h1[0], h1[1]); w.w = cvt_pk_bf16(h1[2], h1[3]);
;                     if (WT && wt) st_wt16(hb + HO + off + bj * HALF, w); else *(u32x4*)(hb + HO + off + bj * HALF) = w;
.LBB0_1345:
	s_or_b64 exec, exec, s[30:31]
	v_add_u32_e32 v106, 0x80, v164
	v_ashrrev_i32_e32 v107, 31, v106
	v_add_u32_e32 v102, 0x90, v164
	v_lshlrev_b64 v[112:113], 11, v[106:107]
	v_ashrrev_i32_e32 v103, 31, v102
	v_add_u32_e32 v98, 0xa0, v164
	v_lshl_add_u64 v[66:67], v[166:167], 0, v[112:113]
	v_lshlrev_b64 v[104:105], 11, v[102:103]
	v_ashrrev_i32_e32 v99, 31, v98
	v_add_u32_e32 v94, 0xb0, v164
	v_mov_b64_e32 v[108:109], v[230:231]
	v_mov_b64_e32 v[110:111], v[232:233]
	v_mov_b64_e32 v[90:91], v[234:235]
	v_mov_b64_e32 v[92:93], v[236:237]
	v_lshl_add_u64 v[66:67], v[166:167], 0, v[104:105]
	v_lshlrev_b64 v[100:101], 11, v[98:99]
	v_ashrrev_i32_e32 v95, 31, v94
	v_mov_b64_e32 v[86:87], v[238:239]
	v_mov_b64_e32 v[88:89], v[240:241]
	v_mov_b64_e32 v[82:83], v[242:243]
	v_mov_b64_e32 v[84:85], v[244:245]
	v_lshl_add_u64 v[66:67], v[166:167], 0, v[100:101]
	v_lshlrev_b64 v[96:97], 11, v[94:95]
	v_mov_b64_e32 v[78:79], v[246:247]
	v_mov_b64_e32 v[80:81], v[248:249]
	v_mov_b64_e32 v[74:75], v[250:251]
	v_mov_b64_e32 v[76:77], v[252:253]
	v_lshl_add_u64 v[66:67], v[166:167], 0, v[96:97]
	v_mov_b64_e32 v[70:71], v[222:223]
	v_mov_b64_e32 v[72:73], v[224:225]
	s_nop 0
	v_mov_b64_e32 v[66:67], v[212:213]
	v_mov_b64_e32 v[68:69], v[214:215]
	v_lshl_add_u64 v[112:113], s[12:13], 0, v[112:113]
	s_and_b64 vcc, exec, s[4:5]
	v_lshl_add_u64 v[112:113], v[162:163], 1, v[112:113]
	v_lshlrev_b32_e32 v114, 16, v108
	v_and_b32_e32 v115, 0xffff0000, v108
	v_lshlrev_b32_e32 v108, 16, v109
	v_and_b32_e32 v109, 0xffff0000, v109
	v_lshlrev_b32_e32 v116, 16, v110
	v_and_b32_e32 v117, 0xffff0000, v110
	v_lshlrev_b32_e32 v118, 16, v111
	v_and_b32_e32 v119, 0xffff0000, v111
	v_pk_add_f32 v[108:109], v[62:63], v[108:109]
	v_pk_add_f32 v[110:111], v[60:61], v[114:115]
	v_pk_add_f32 v[60:61], v[58:59], v[118:119]
	v_pk_add_f32 v[62:63], v[56:57], v[116:117]
	v_cvt_pk_bf16_f32 v56, v110, v111
	v_cvt_pk_bf16_f32 v57, v108, v109
	s_nop 0
	v_cvt_pk_bf16_f32 v58, v62, v63
	v_cvt_pk_bf16_f32 v59, v60, v61
	s_cbranch_vccnz .LBB0_1399
	global_store_dwordx4 v[112:113], v[56:59], off
	s_cbranch_execnz .LBB0_1348

; __device__ __forceinline__ unsigned cvt_pk_bf16(float lo, float hi) { unsigned r; asm volatile("v_cvt_pk_bf16_f32 %0, %1, %2" : "=v"(r) : "v"(lo), "v"(hi)); return r; }
; __device__ __forceinline__ void st_wt16(void* p, u32x4 v) { asm volatile("global_store_dwordx4 %0, %1, off sc1\n\ts_nop 1" :: "v"(p), "v"(v) : "memory"); }
;     __device__ __forceinline__ void operator()(const f32x4 (&acc)[2][2][4][2], const Unit& u, int wr, int wc, int fr, int fq) const {
;     ...
;                     else { const u32x4 b = bb[m][bj];
;                         h0 = (f32x4){__uint_as_float(b.x << 16), __uint_as_float(b.x & 0xffff0000u), __uint_as_float(b.y << 16), __uint_as_float(b.y & 0xffff0000u)};
;                         h1 = (f32x4){__uint_as_float(b.z << 16), __uint_as_float(b.z & 0xffff0000u), __uint_as_float(b.w << 16), __uint_as_float(b.w & 0xffff0000u)}; }
;                     h0 = h0 + acc[ai][bj][m][0]; h1 = h1 + acc[ai][bj][m][1];
;                     u32x4 w; w.x = cvt_pk_bf16(h0[0], h0[1]); w.y = cvt_pk_bf16(h0[2], h0[3]); w.z = cvt_pk_bf16(h1[0], h1[1]); w.w = cvt_pk_bf16(h1[2], h1[3]);
;                     if (WT && wt) st_wt16(hb + HO + off + bj * HALF, w); else *(u32x4*)(hb + HO + off + bj * HALF) = w;
.LBB0_1355:
	s_or_b64 exec, exec, s[30:31]
	v_lshlrev_b32_e32 v50, 16, v87
	v_and_b32_e32 v51, 0xffff0000, v87
	v_lshlrev_b32_e32 v52, 16, v88
	v_and_b32_e32 v53, 0xffff0000, v88
	v_lshlrev_b32_e32 v48, 16, v86
	v_and_b32_e32 v49, 0xffff0000, v86
	v_lshlrev_b32_e32 v54, 16, v89
	v_and_b32_e32 v55, 0xffff0000, v89
	v_pk_add_f32 v[38:39], v[38:39], v[50:51]
	v_pk_add_f32 v[50:51], v[32:33], v[52:53]
	v_lshl_add_u64 v[52:53], s[12:13], 0, v[104:105]
	v_pk_add_f32 v[48:49], v[36:37], v[48:49]
	v_pk_add_f32 v[36:37], v[34:35], v[54:55]
	s_and_b64 vcc, exec, s[4:5]
	v_lshl_add_u64 v[52:53], v[162:163], 1, v[52:53]
	v_cvt_pk_bf16_f32 v32, v48, v49
	v_cvt_pk_bf16_f32 v33, v38, v39
	v_cvt_pk_bf16_f32 v34, v50, v51
	v_cvt_pk_bf16_f32 v35, v36, v37
	s_cbranch_vccnz .LBB0_1401
	global_store_dwordx4 v[52:53], v[32:35], off
	s_cbranch_execnz .LBB0_1358

; __device__ __forceinline__ unsigned cvt_pk_bf16(float lo, float hi) { unsigned r; asm volatile("v_cvt_pk_bf16_f32 %0, %1, %2" : "=v"(r) : "v"(lo), "v"(hi)); return r; }
; __device__ __forceinline__ void st_wt16(void* p, u32x4 v) { asm volatile("global_store_dwordx4 %0, %1, off sc1\n\ts_nop 1" :: "v"(p), "v"(v) : "memory"); }
;     __device__ __forceinline__ void operator()(const f32x4 (&acc)[2][2][4][2], const Unit& u, int wr, int wc, int fr, int fq) const {
;     ...
;                     else { const u32x4 b = bb[m][bj];
;                         h0 = (f32x4){__uint_as_float(b.x << 16), __uint_as_float(b.x & 0xffff0000u), __uint_as_float(b.y << 16), __uint_as_float(b.y & 0xffff0000u)};
;                         h1 = (f32x4){__uint_as_float(b.z << 16), __uint_as_float(b.z & 0xffff0000u), __uint_as_float(b.w << 16), __uint_as_float(b.w & 0xffff0000u)}; }
;                     h0 = h0 + acc[ai][bj][m][0]; h1 = h1 + acc[ai][bj][m][1];
;                     u32x4 w; w.x = cvt_pk_bf16(h0[0], h0[1]); w.y = cvt_pk_bf16(h0[2], h0[3]); w.z = cvt_pk_bf16(h1[0], h1[1]); w.w = cvt_pk_bf16(h1[2], h1[3]);
;                     if (WT && wt) st_wt16(hb + HO + off + bj * HALF, w); else *(u32x4*)(hb + HO + off + bj * HALF) = w;
.LBB0_1365:
	s_or_b64 exec, exec, s[30:31]
	v_lshlrev_b32_e32 v34, 16, v79
	v_and_b32_e32 v35, 0xffff0000, v79
	v_lshlrev_b32_e32 v36, 16, v80
	v_and_b32_e32 v37, 0xffff0000, v80
	v_lshlrev_b32_e32 v32, 16, v78
	v_and_b32_e32 v33, 0xffff0000, v78
	v_lshlrev_b32_e32 v38, 16, v81
	v_and_b32_e32 v39, 0xffff0000, v81
	v_pk_add_f32 v[22:23], v[22:23], v[34:35]
	v_pk_add_f32 v[34:35], v[16:17], v[36:37]
	v_lshl_add_u64 v[36:37], s[12:13], 0, v[100:101]
	v_pk_add_f32 v[32:33], v[20:21], v[32:33]
	v_pk_add_f32 v[20:21], v[18:19], v[38:39]
	s_and_b64 vcc, exec, s[4:5]
	v_lshl_add_u64 v[36:37], v[162:163], 1, v[36:37]
	v_cvt_pk_bf16_f32 v16, v32, v33
	v_cvt_pk_bf16_f32 v17, v22, v23
	v_cvt_pk_bf16_f32 v18, v34, v35
	v_cvt_pk_bf16_f32 v19, v20, v21
	s_cbranch_vccnz .LBB0_1403
	global_store_dwordx4 v[36:37], v[16:19], off
	s_cbranch_execnz .LBB0_1368

; __device__ __forceinline__ unsigned cvt_pk_bf16(float lo, float hi) { unsigned r; asm volatile("v_cvt_pk_bf16_f32 %0, %1, %2" : "=v"(r) : "v"(lo), "v"(hi)); return r; }
; __device__ __forceinline__ void st_wt16(void* p, u32x4 v) { asm volatile("global_store_dwordx4 %0, %1, off sc1\n\ts_nop 1" :: "v"(p), "v"(v) : "memory"); }
;     __device__ __forceinline__ void operator()(const f32x4 (&acc)[2][2][4][2], const Unit& u, int wr, int wc, int fr, int fq) const {
;     ...
;                     else { const u32x4 b = bb[m][bj];
;                         h0 = (f32x4){__uint_as_float(b.x << 16), __uint_as_float(b.x & 0xffff0000u), __uint_as_float(b.y << 16), __uint_as_float(b.y & 0xffff0000u)};
;                         h1 = (f32x4){__uint_as_float(b.z << 16), __uint_as_float(b.z & 0xffff0000u), __uint_as_float(b.w << 16), __uint_as_float(b.w & 0xffff0000u)}; }
;                     h0 = h0 + acc[ai][bj][m][0]; h1 = h1 + acc[ai][bj][m][1];
;                     u32x4 w; w.x = cvt_pk_bf16(h0[0], h0[1]); w.y = cvt_pk_bf16(h0[2], h0[3]); w.z = cvt_pk_bf16(h1[0], h1[1]); w.w = cvt_pk_bf16(h1[2], h1[3]);
;                     if (WT && wt) st_wt16(hb + HO + off + bj * HALF, w); else *(u32x4*)(hb + HO + off + bj * HALF) = w;
.LBB0_1375:
	s_or_b64 exec, exec, s[30:31]
	v_lshlrev_b32_e32 v18, 16, v71
	v_and_b32_e32 v19, 0xffff0000, v71
	v_lshlrev_b32_e32 v20, 16, v72
	v_and_b32_e32 v21, 0xffff0000, v72
	v_lshlrev_b32_e32 v16, 16, v70
	v_and_b32_e32 v17, 0xffff0000, v70
	v_lshlrev_b32_e32 v22, 16, v73
	v_and_b32_e32 v23, 0xffff0000, v73
	v_pk_add_f32 v[6:7], v[6:7], v[18:19]
	v_pk_add_f32 v[18:19], v[0:1], v[20:21]
	v_lshl_add_u64 v[20:21], s[12:13], 0, v[96:97]
	v_pk_add_f32 v[16:17], v[4:5], v[16:17]
	v_pk_add_f32 v[4:5], v[2:3], v[22:23]
	s_and_b64 vcc, exec, s[4:5]
	v_lshl_add_u64 v[20:21], v[162:163], 1, v[20:21]
	v_cvt_pk_bf16_f32 v0, v16, v17
	v_cvt_pk_bf16_f32 v1, v6, v7
	v_cvt_pk_bf16_f32 v2, v18, v19
	v_cvt_pk_bf16_f32 v3, v4, v5
	s_cbranch_vccnz .LBB0_1405
	global_store_dwordx4 v[20:21], v[0:3], off
	s_cbranch_execnz .LBB0_1378
